# phase 10 combine: two grid-stride iterations per trip (10 loads per lane in flight), on top of the phase-0 and router edits
# speedup vs baseline: 1.0089x; 1.0089x over previous
.LBB0_1147:
	s_cmp_lt_i32 s78, 11
	s_cselect_b64 s[4:5], -1, 0
	s_and_b64 s[8:9], s[4:5], s[6:7]
	s_andn2_b64 vcc, exec, s[8:9]
	s_cbranch_vccnz .LBB0_1152
	s_mov_b32 s3, 0
	s_lshl_b64 s[4:5], s[2:3], 9
	v_or_b32_e32 v2, s4, v250
	v_mov_b32_e32 v3, s5
	s_mov_b64 s[4:5], 0x200000
	v_cmp_gt_u64_e32 vcc, s[4:5], v[2:3]
	s_and_saveexec_b64 s[10:11], vcc
	s_cbranch_execz .LBB0_1151
	s_load_dwordx4 s[4:7], s[0:1], 0xc8
	s_lshl_b64 s[14:15], s[2:3], 13
	s_mov_b32 s81, s3
	s_lshl_b64 s[12:13], s[2:3], 12
	v_lshl_or_b32 v0, v250, 4, s14
	v_mov_b32_e32 v1, s15
	s_mov_b64 s[14:15], 0x31d78000
	s_waitcnt lgkmcnt(0)
	s_lshl_b64 s[0:1], s[80:81], 9
	s_waitcnt vmcnt(0)
	v_lshl_or_b32 v6, v250, 3, s12
	v_mov_b32_e32 v7, s13
	s_lshl_b64 s[12:13], s[80:81], 12
	v_lshl_add_u64 v[8:9], v[0:1], 0, s[14:15]
	s_lshl_b64 s[14:15], s[80:81], 13
	s_lshl_b64 s[2:3], s[2:3], 14
	s_add_u32 s2, s4, s2
	v_mov_b32_e32 v5, 0
	v_lshlrev_b32_e32 v4, 5, v250
	s_addc_u32 s3, s5, s3
	v_lshl_add_u64 v[0:1], s[2:3], 0, v[4:5]
	v_lshl_add_u64 v[10:11], v[0:1], 0, 16
	s_lshl_b64 s[2:3], s[80:81], 14
	s_mov_b64 s[4:5], 0
	s_mov_b32 s19, 0xc000
	v_mov_b64_e32 v[12:13], s[6:7]
	s_mov_b64 s[16:17], 0x12000
	s_mov_b32 s22, 0x12000
	s_mov_b32 s18, 0x3d800000
	s_mov_b64 s[20:21], 0x1fffff
	s_cmp_eq_u32 s80, 0x100
	s_cbranch_scc0 .LBB0_1150
	v_mov_b32_e32 v55, 0
.Lp10_fast:
	v_lshl_add_u64 v[0:1], s[6:7], 0, v[6:7]
	v_alignbit_b32 v19, v3, v2, 19
	v_add_co_u32_e32 v18, vcc, 0x2dd78000, v0
	v_mad_u64_u32 v[20:21], s[24:25], v19, s19, v[12:13]
	s_nop 0
	v_addc_co_u32_e32 v19, vcc, 0, v1, vcc
	v_add_co_u32_e32 v0, vcc, 0x2ed78000, v0
	v_lshl_add_u64 v[14:15], s[6:7], 0, v[8:9]
	s_nop 0
	v_addc_co_u32_e32 v1, vcc, 0, v1, vcc
	v_and_b32_e32 v4, 0x7f8, v6
	v_lshrrev_b32_e32 v22, 19, v3
	global_load_dwordx4 v[14:17], v[14:15], off nt
	v_lshlrev_b32_e32 v4, 2, v4
	global_load_dwordx2 v[26:27], v[18:19], off nt
	v_mad_u32_u24 v21, v22, s19, v21
	global_load_dwordx2 v[0:1], v[0:1], off nt
	v_lshl_add_u64 v[18:19], v[20:21], 0, v[4:5]
	v_add_co_u32_e32 v30, vcc, s22, v18
	v_lshl_add_u64 v[28:29], v[18:19], 0, s[16:17]
	s_nop 0
	v_addc_co_u32_e32 v31, vcc, 0, v19, vcc
	global_load_dwordx4 v[18:21], v[30:31], off
	global_load_dwordx4 v[22:25], v[28:29], off offset:16
	v_lshl_add_u64 v[2:3], v[2:3], 0, s[0:1]
	v_cmp_lt_u64_e32 vcc, s[20:21], v[2:3]
	v_lshl_add_u64 v[6:7], v[6:7], 0, s[12:13]
	v_lshl_add_u64 v[8:9], v[8:9], 0, s[14:15]
	s_or_b64 s[4:5], vcc, s[4:5]
	v_lshl_add_u64 v[50:51], s[6:7], 0, v[6:7]
	v_alignbit_b32 v69, v3, v2, 19
	v_add_co_u32_e32 v68, vcc, 0x2dd78000, v50
	v_mad_u64_u32 v[70:71], s[24:25], v69, s19, v[12:13]
	s_nop 0
	v_addc_co_u32_e32 v69, vcc, 0, v51, vcc
	v_add_co_u32_e32 v50, vcc, 0x2ed78000, v50
	v_lshl_add_u64 v[64:65], s[6:7], 0, v[8:9]
	s_nop 0
	v_addc_co_u32_e32 v51, vcc, 0, v51, vcc
	v_and_b32_e32 v54, 0x7f8, v6
	v_lshrrev_b32_e32 v72, 19, v3
	global_load_dwordx4 v[64:67], v[64:65], off nt
	v_lshlrev_b32_e32 v54, 2, v54
	global_load_dwordx2 v[76:77], v[68:69], off nt
	v_mad_u32_u24 v71, v72, s19, v71
	global_load_dwordx2 v[50:51], v[50:51], off nt
	v_lshl_add_u64 v[68:69], v[70:71], 0, v[54:55]
	v_add_co_u32_e32 v80, vcc, s22, v68
	v_lshl_add_u64 v[78:79], v[68:69], 0, s[16:17]
	s_nop 0
	v_addc_co_u32_e32 v81, vcc, 0, v69, vcc
	global_load_dwordx4 v[68:71], v[80:81], off
	global_load_dwordx4 v[72:75], v[78:79], off offset:16
	v_lshl_add_u64 v[2:3], v[2:3], 0, s[0:1]
	v_cmp_lt_u64_e32 vcc, s[20:21], v[2:3]
	v_lshl_add_u64 v[6:7], v[6:7], 0, s[12:13]
	v_lshl_add_u64 v[8:9], v[8:9], 0, s[14:15]
	s_or_b64 s[4:5], vcc, s[4:5]
	s_waitcnt vmcnt(9)
	v_lshlrev_b32_e32 v28, 16, v14
	v_and_b32_e32 v29, 0xffff0000, v14
	v_lshlrev_b32_e32 v30, 16, v15
	v_and_b32_e32 v31, 0xffff0000, v15
	v_lshlrev_b32_e32 v32, 16, v16
	v_and_b32_e32 v33, 0xffff0000, v16
	v_lshlrev_b32_e32 v34, 16, v17
	v_and_b32_e32 v35, 0xffff0000, v17
	s_waitcnt vmcnt(8)
	v_cvt_pk_f32_fp8_e32 v[14:15], v26
	v_cvt_pk_f32_fp8_sdwa v[16:17], v26 src0_sel:WORD_1
	s_waitcnt vmcnt(7)
	v_cvt_pk_f32_fp8_e32 v[38:39], v0
	v_cvt_pk_f32_fp8_sdwa v[40:41], v0 src0_sel:WORD_1
	v_cvt_pk_f32_fp8_e32 v[36:37], v27
	v_cvt_pk_f32_fp8_sdwa v[26:27], v27 src0_sel:WORD_1
	v_cvt_pk_f32_fp8_e32 v[42:43], v1
	v_cvt_pk_f32_fp8_sdwa v[0:1], v1 src0_sel:WORD_1
	s_waitcnt vmcnt(6)
	v_pk_mul_f32 v[20:21], v[20:21], s[18:19] op_sel_hi:[1,0]
	v_pk_mul_f32 v[18:19], v[18:19], s[18:19] op_sel_hi:[1,0]
	v_pk_add_f32 v[14:15], v[14:15], v[38:39]
	v_pk_add_f32 v[16:17], v[16:17], v[40:41]
	s_waitcnt vmcnt(5)
	v_pk_mul_f32 v[24:25], v[24:25], s[18:19] op_sel_hi:[1,0]
	v_pk_mul_f32 v[22:23], v[22:23], s[18:19] op_sel_hi:[1,0]
	v_pk_add_f32 v[36:37], v[36:37], v[42:43]
	v_pk_add_f32 v[0:1], v[26:27], v[0:1]
	v_pk_fma_f32 v[14:15], v[14:15], v[18:19], v[28:29]
	v_pk_fma_f32 v[16:17], v[16:17], v[20:21], v[30:31]
	v_pk_fma_f32 v[18:19], v[36:37], v[22:23], v[32:33]
	v_pk_fma_f32 v[20:21], v[0:1], v[24:25], v[34:35]
	global_store_dwordx4 v[10:11], v[14:17], off offset:-16 nt
	global_store_dwordx4 v[10:11], v[18:21], off nt
	v_lshl_add_u64 v[10:11], v[10:11], 0, s[2:3]
	s_waitcnt vmcnt(6)
	v_lshlrev_b32_e32 v78, 16, v64
	v_and_b32_e32 v79, 0xffff0000, v64
	v_lshlrev_b32_e32 v80, 16, v65
	v_and_b32_e32 v81, 0xffff0000, v65
	v_lshlrev_b32_e32 v82, 16, v66
	v_and_b32_e32 v83, 0xffff0000, v66
	v_lshlrev_b32_e32 v84, 16, v67
	v_and_b32_e32 v85, 0xffff0000, v67
	s_waitcnt vmcnt(5)
	v_cvt_pk_f32_fp8_e32 v[64:65], v76
	v_cvt_pk_f32_fp8_sdwa v[66:67], v76 src0_sel:WORD_1
	s_waitcnt vmcnt(4)
	v_cvt_pk_f32_fp8_e32 v[88:89], v50
	v_cvt_pk_f32_fp8_sdwa v[90:91], v50 src0_sel:WORD_1
	v_cvt_pk_f32_fp8_e32 v[86:87], v77
	v_cvt_pk_f32_fp8_sdwa v[76:77], v77 src0_sel:WORD_1
	v_cvt_pk_f32_fp8_e32 v[92:93], v51
	v_cvt_pk_f32_fp8_sdwa v[50:51], v51 src0_sel:WORD_1
	s_waitcnt vmcnt(3)
	v_pk_mul_f32 v[70:71], v[70:71], s[18:19] op_sel_hi:[1,0]
	v_pk_mul_f32 v[68:69], v[68:69], s[18:19] op_sel_hi:[1,0]
	v_pk_add_f32 v[64:65], v[64:65], v[88:89]
	v_pk_add_f32 v[66:67], v[66:67], v[90:91]
	s_waitcnt vmcnt(2)
	v_pk_mul_f32 v[74:75], v[74:75], s[18:19] op_sel_hi:[1,0]
	v_pk_mul_f32 v[72:73], v[72:73], s[18:19] op_sel_hi:[1,0]
	v_pk_add_f32 v[86:87], v[86:87], v[92:93]
	v_pk_add_f32 v[50:51], v[76:77], v[50:51]
	v_pk_fma_f32 v[64:65], v[64:65], v[68:69], v[78:79]
	v_pk_fma_f32 v[66:67], v[66:67], v[70:71], v[80:81]
	v_pk_fma_f32 v[68:69], v[86:87], v[72:73], v[82:83]
	v_pk_fma_f32 v[70:71], v[50:51], v[74:75], v[84:85]
	global_store_dwordx4 v[10:11], v[64:67], off offset:-16 nt
	global_store_dwordx4 v[10:11], v[68:71], off nt
	v_lshl_add_u64 v[10:11], v[10:11], 0, s[2:3]
	s_andn2_b64 exec, exec, s[4:5]
	s_cbranch_execnz .Lp10_fast
	s_branch .LBB0_1151
